# stream: staggered start of wave groups (s_sleep ladder, 0/0.16/0.32/0.48us) on top of rotated wave-row assignment
# baseline (speedup 1.0000x reference)
.LBB1_2:
	s_or_b64 exec, exec, s[0:1]
	s_lshr_b32 s8, s3, 6
	s_lshr_b32 s11, s8, 2
	s_cmp_lt_u32 s11, 1
	s_cbranch_scc1 .Lst_go
	s_sleep 6
	s_cmp_lt_u32 s11, 2
	s_cbranch_scc1 .Lst_go
	s_sleep 6
	s_cmp_lt_u32 s11, 3
	s_cbranch_scc1 .Lst_go
	s_sleep 6
.Lst_go:
	s_add_i32 s8, s8, s2
	s_and_b32 s8, s8, 15
	s_lshl_b32 s0, s2, 7
	v_and_b32_e32 v24, 63, v0
	s_add_i32 s9, s8, s0
	s_waitcnt lgkmcnt(0)
	s_and_b32 s1, s5, 0xffff
	s_mov_b32 s3, 0x20000
	s_brev_b32 s2, 16
	s_mov_b32 s0, s4
	v_lshlrev_b32_e32 v25, 4, v24
	s_lshl_b32 s4, s9, 12
	buffer_load_dwordx4 v[26:29], v25, s[0:3], s4 offen offset:1024 nt
	buffer_load_dwordx4 v[30:33], v25, s[0:3], s4 offen nt
	buffer_load_dwordx4 v[34:37], v25, s[0:3], s4 offen offset:2048 nt
	s_add_i32 s5, s4, 0x10000
	buffer_load_dwordx4 v[38:41], v25, s[0:3], s5 offen offset:1024 nt
	buffer_load_dwordx4 v[42:45], v25, s[0:3], s5 offen nt
	buffer_load_dwordx4 v[16:19], v25, s[0:3], s4 offen offset:3072 nt
	s_add_i32 s10, s4, 0x20000
	buffer_load_dwordx4 v[46:49], v25, s[0:3], s5 offen offset:2048 nt
	buffer_load_dwordx4 v[20:23], v25, s[0:3], s5 offen offset:3072 nt
	s_barrier
	buffer_load_dwordx4 v[50:53], v25, s[0:3], s10 offen offset:1024 nt
	buffer_load_dwordx4 v[54:57], v25, s[0:3], s10 offen nt
	ds_read_b128 v[4:7], v25 offset:1024
	ds_read_b128 v[0:3], v25
	ds_read_b128 v[12:15], v25 offset:2048
	ds_read_b128 v[8:11], v25 offset:3072
	s_add_i32 s5, s4, 0x30000
	v_cmp_gt_u32_e32 vcc, 8, v24
	s_waitcnt vmcnt(9) lgkmcnt(3)
	v_pk_mul_f32 v[28:29], v[6:7], v[28:29]
	v_pk_mul_f32 v[26:27], v[4:5], v[26:27]
	s_waitcnt vmcnt(8) lgkmcnt(2)
	v_pk_fma_f32 v[32:33], v[2:3], v[32:33], v[28:29]
	v_pk_fma_f32 v[30:31], v[0:1], v[30:31], v[26:27]
	buffer_load_dwordx4 v[26:29], v25, s[0:3], s5 offen offset:1024 nt
	s_waitcnt vmcnt(8) lgkmcnt(1)
	v_pk_fma_f32 v[58:59], v[14:15], v[36:37], v[32:33]
	v_pk_fma_f32 v[60:61], v[12:13], v[34:35], v[30:31]
	buffer_load_dwordx4 v[30:33], v25, s[0:3], s5 offen nt
	s_waitcnt vmcnt(8)
	v_pk_mul_f32 v[34:35], v[6:7], v[40:41]
	v_pk_mul_f32 v[36:37], v[4:5], v[38:39]
	s_waitcnt vmcnt(7)
	v_pk_fma_f32 v[44:45], v[2:3], v[44:45], v[34:35]
	v_pk_fma_f32 v[42:43], v[0:1], v[42:43], v[36:37]
	buffer_load_dwordx4 v[34:37], v25, s[0:3], s10 offen offset:2048 nt
	s_waitcnt vmcnt(4)
	v_pk_mul_f32 v[38:39], v[6:7], v[52:53]
	v_pk_mul_f32 v[40:41], v[4:5], v[50:51]
	s_waitcnt vmcnt(3)
	v_pk_fma_f32 v[50:51], v[2:3], v[56:57], v[38:39]
	v_pk_fma_f32 v[52:53], v[0:1], v[54:55], v[40:41]
	buffer_load_dwordx4 v[38:41], v25, s[0:3], s10 offen offset:3072 nt
	v_pk_fma_f32 v[48:49], v[14:15], v[48:49], v[44:45]
	v_pk_fma_f32 v[46:47], v[12:13], v[46:47], v[42:43]
	s_waitcnt lgkmcnt(0)
	v_pk_fma_f32 v[18:19], v[10:11], v[18:19], v[58:59]
	v_pk_fma_f32 v[16:17], v[8:9], v[16:17], v[60:61]
	v_add_f32_e32 v61, v18, v19
	v_add_f32_e32 v60, v16, v17
	v_pk_fma_f32 v[16:17], v[10:11], v[22:23], v[48:49]
	v_pk_fma_f32 v[18:19], v[8:9], v[20:21], v[46:47]
	v_add_f32_e32 v16, v16, v17
	v_add_f32_e32 v18, v18, v19
	v_add_f32_e32 v60, v60, v61
	v_add_f32_e32 v16, v18, v16
	s_add_i32 s10, s4, 0x50000
	s_waitcnt vmcnt(3)
	v_pk_mul_f32 v[28:29], v[6:7], v[28:29]
	v_pk_mul_f32 v[26:27], v[4:5], v[26:27]
	v_add_f32_dpp v16, v16, v16 quad_perm:[1,0,3,2] row_mask:0xf bank_mask:0xf bound_ctrl:1
	s_waitcnt vmcnt(2)
	v_pk_fma_f32 v[54:55], v[2:3], v[32:33], v[28:29]
	v_pk_fma_f32 v[56:57], v[0:1], v[30:31], v[26:27]
	buffer_load_dwordx4 v[26:29], v25, s[0:3], s5 offen offset:2048 nt
	buffer_load_dwordx4 v[30:33], v25, s[0:3], s5 offen offset:3072 nt
	s_add_i32 s5, s4, 0x40000
	buffer_load_dwordx4 v[42:45], v25, s[0:3], s5 offen offset:1024 nt
	s_waitcnt vmcnt(4)
	v_pk_fma_f32 v[50:51], v[14:15], v[36:37], v[50:51]
	v_pk_fma_f32 v[52:53], v[12:13], v[34:35], v[52:53]
	buffer_load_dwordx4 v[34:37], v25, s[0:3], s5 offen nt
	v_add_f32_dpp v16, v16, v16 quad_perm:[2,3,0,1] row_mask:0xf bank_mask:0xf bound_ctrl:1
	s_waitcnt vmcnt(4)
	v_pk_fma_f32 v[58:59], v[10:11], v[40:41], v[50:51]
	v_pk_fma_f32 v[38:39], v[8:9], v[38:39], v[52:53]
	v_add_f32_e32 v19, v58, v59
	v_add_f32_e32 v17, v38, v39
	v_add_f32_dpp v58, v60, v60 quad_perm:[1,0,3,2] row_mask:0xf bank_mask:0xf bound_ctrl:1
	v_add_f32_e32 v18, v17, v19
	v_add_f32_dpp v16, v16, v16 row_ror:4 row_mask:0xf bank_mask:0xf bound_ctrl:1
	v_add_f32_dpp v17, v58, v58 quad_perm:[2,3,0,1] row_mask:0xf bank_mask:0xf bound_ctrl:1
	buffer_load_dwordx4 v[20:23], v25, s[0:3], s5 offen offset:2048 nt
	buffer_load_dwordx4 v[46:49], v25, s[0:3], s5 offen offset:3072 nt
	v_add_f32_dpp v17, v17, v17 row_ror:4 row_mask:0xf bank_mask:0xf bound_ctrl:1
	v_add_f32_dpp v58, v16, v16 row_ror:8 row_mask:0xf bank_mask:0xf bound_ctrl:1
	buffer_load_dwordx4 v[38:41], v25, s[0:3], s10 offen nt
	buffer_load_dwordx4 v[50:53], v25, s[0:3], s10 offen offset:1024 nt
	v_add_f32_dpp v17, v17, v17 row_ror:8 row_mask:0xf bank_mask:0xf bound_ctrl:1
	v_mov_b32_e32 v19, v17
	v_mov_b32_e32 v59, v58
	s_nop 0
	v_permlane16_swap_b32_e32 v17, v19
	v_permlane16_swap_b32_e32 v58, v59
	v_add_f32_e32 v16, v17, v19
	v_add_f32_e32 v17, v58, v59
	s_add_i32 s5, s4, 0x60000
	s_add_i32 s4, s4, 0x70000
	v_add_f32_dpp v18, v18, v18 quad_perm:[1,0,3,2] row_mask:0xf bank_mask:0xf bound_ctrl:1
	s_waitcnt vmcnt(7)
	v_pk_fma_f32 v[28:29], v[14:15], v[28:29], v[54:55]
	v_pk_fma_f32 v[54:55], v[12:13], v[26:27], v[56:57]
	s_waitcnt vmcnt(6)
	v_pk_fma_f32 v[58:59], v[10:11], v[32:33], v[28:29]
	buffer_load_dwordx4 v[26:29], v25, s[0:3], s10 offen offset:2048 nt
	v_pk_fma_f32 v[54:55], v[8:9], v[30:31], v[54:55]
	buffer_load_dwordx4 v[30:33], v25, s[0:3], s10 offen offset:3072 nt
	v_add_f32_e32 v66, v54, v55
	s_waitcnt vmcnt(7)
	v_pk_mul_f32 v[54:55], v[6:7], v[44:45]
	v_pk_mul_f32 v[56:57], v[4:5], v[42:43]
	buffer_load_dwordx4 v[42:45], v25, s[0:3], s5 offen offset:1024 nt
	s_waitcnt vmcnt(7)
	v_pk_fma_f32 v[54:55], v[2:3], v[36:37], v[54:55]
	v_pk_fma_f32 v[56:57], v[0:1], v[34:35], v[56:57]
	buffer_load_dwordx4 v[34:37], v25, s[0:3], s5 offen nt
	v_add_f32_dpp v18, v18, v18 quad_perm:[2,3,0,1] row_mask:0xf bank_mask:0xf bound_ctrl:1
	s_waitcnt vmcnt(7)
	v_pk_fma_f32 v[22:23], v[14:15], v[22:23], v[54:55]
	v_pk_fma_f32 v[20:21], v[12:13], v[20:21], v[56:57]
	s_waitcnt vmcnt(6)
	v_pk_fma_f32 v[60:61], v[10:11], v[48:49], v[22:23]
	v_pk_fma_f32 v[22:23], v[8:9], v[46:47], v[20:21]
	s_waitcnt vmcnt(4)
	v_pk_mul_f32 v[54:55], v[4:5], v[50:51]
	v_pk_mul_f32 v[20:21], v[6:7], v[52:53]
	v_pk_fma_f32 v[38:39], v[0:1], v[38:39], v[54:55]
	buffer_load_dwordx4 v[46:49], v25, s[0:3], s5 offen offset:2048 nt
	buffer_load_dwordx4 v[50:53], v25, s[0:3], s5 offen offset:3072 nt
	v_pk_fma_f32 v[20:21], v[2:3], v[40:41], v[20:21]
	v_add_f32_e32 v23, v22, v23
	v_add_f32_dpp v18, v18, v18 row_ror:4 row_mask:0xf bank_mask:0xf bound_ctrl:1
	s_waitcnt vmcnt(5)
	v_pk_fma_f32 v[26:27], v[12:13], v[26:27], v[38:39]
	buffer_load_dwordx4 v[38:41], v25, s[0:3], s4 offen nt
	buffer_load_dwordx4 v[54:57], v25, s[0:3], s4 offen offset:1024 nt
	v_pk_fma_f32 v[20:21], v[14:15], v[28:29], v[20:21]
	s_waitcnt vmcnt(6)
	v_pk_fma_f32 v[30:31], v[8:9], v[30:31], v[26:27]
	v_pk_fma_f32 v[62:63], v[10:11], v[32:33], v[20:21]
	v_add_f32_dpp v18, v18, v18 row_ror:8 row_mask:0xf bank_mask:0xf bound_ctrl:1
	s_waitcnt vmcnt(5)
	v_pk_mul_f32 v[20:21], v[6:7], v[44:45]
	v_pk_mul_f32 v[26:27], v[4:5], v[42:43]
	buffer_load_dwordx4 v[42:45], v25, s[0:3], s4 offen offset:2048 nt
	s_waitcnt vmcnt(5)
	v_pk_fma_f32 v[64:65], v[0:1], v[34:35], v[26:27]
	buffer_load_dwordx4 v[32:35], v25, s[0:3], s4 offen offset:3072 nt
	v_add_f32_e32 v27, v60, v61
	v_add_f32_e32 v23, v23, v27
	v_pk_fma_f32 v[36:37], v[2:3], v[36:37], v[20:21]
	v_add_f32_e32 v20, v58, v59
	v_add_f32_dpp v23, v23, v23 quad_perm:[1,0,3,2] row_mask:0xf bank_mask:0xf bound_ctrl:1
	v_add_f32_e32 v20, v66, v20
	v_mov_b32_e32 v19, v18
	v_add_f32_dpp v23, v23, v23 quad_perm:[2,3,0,1] row_mask:0xf bank_mask:0xf bound_ctrl:1
	v_add_f32_dpp v20, v20, v20 quad_perm:[1,0,3,2] row_mask:0xf bank_mask:0xf bound_ctrl:1
	v_permlane16_swap_b32_e32 v18, v19
	v_add_f32_dpp v23, v23, v23 row_ror:4 row_mask:0xf bank_mask:0xf bound_ctrl:1
	v_add_f32_dpp v20, v20, v20 quad_perm:[2,3,0,1] row_mask:0xf bank_mask:0xf bound_ctrl:1
	v_add_f32_e32 v18, v18, v19
	v_add_f32_dpp v23, v23, v23 row_ror:8 row_mask:0xf bank_mask:0xf bound_ctrl:1
	v_mov_b32_e32 v27, v23
	s_nop 1
	v_permlane16_swap_b32_e32 v23, v27
	v_add_f32_e32 v28, v23, v27
	v_add_f32_e32 v23, v30, v31
	s_waitcnt vmcnt(5)
	v_pk_fma_f32 v[30:31], v[14:15], v[48:49], v[36:37]
	v_pk_fma_f32 v[36:37], v[12:13], v[46:47], v[64:65]
	s_waitcnt vmcnt(4)
	v_pk_fma_f32 v[30:31], v[10:11], v[52:53], v[30:31]
	v_pk_fma_f32 v[36:37], v[8:9], v[50:51], v[36:37]
	v_add_f32_e32 v27, v62, v63
	v_add_f32_e32 v36, v36, v37
	v_add_f32_e32 v30, v30, v31
	v_add_f32_e32 v23, v23, v27
	v_add_f32_e32 v30, v36, v30
	v_add_f32_dpp v20, v20, v20 row_ror:4 row_mask:0xf bank_mask:0xf bound_ctrl:1
	v_add_f32_dpp v23, v23, v23 quad_perm:[1,0,3,2] row_mask:0xf bank_mask:0xf bound_ctrl:1
	v_add_f32_dpp v30, v30, v30 quad_perm:[1,0,3,2] row_mask:0xf bank_mask:0xf bound_ctrl:1
	v_add_f32_dpp v20, v20, v20 row_ror:8 row_mask:0xf bank_mask:0xf bound_ctrl:1
	v_add_f32_dpp v23, v23, v23 quad_perm:[2,3,0,1] row_mask:0xf bank_mask:0xf bound_ctrl:1
	v_add_f32_dpp v30, v30, v30 quad_perm:[2,3,0,1] row_mask:0xf bank_mask:0xf bound_ctrl:1
	v_mov_b32_e32 v21, v20
	v_add_f32_dpp v23, v23, v23 row_ror:4 row_mask:0xf bank_mask:0xf bound_ctrl:1
	v_add_f32_dpp v30, v30, v30 row_ror:4 row_mask:0xf bank_mask:0xf bound_ctrl:1
	v_permlane16_swap_b32_e32 v20, v21
	v_add_f32_dpp v23, v23, v23 row_ror:8 row_mask:0xf bank_mask:0xf bound_ctrl:1
	v_add_f32_dpp v30, v30, v30 row_ror:8 row_mask:0xf bank_mask:0xf bound_ctrl:1
	v_mov_b32_e32 v27, v23
	v_mov_b32_e32 v31, v30
	s_nop 0
	v_permlane16_swap_b32_e32 v23, v27
	v_permlane16_swap_b32_e32 v30, v31
	v_add_f32_e32 v21, v20, v21
	v_add_f32_e32 v23, v23, v27
	v_add_f32_e32 v30, v30, v31
	v_mov_b32_e32 v19, v16
	v_mov_b32_e32 v20, v17
	v_mov_b32_e32 v22, v18
	v_mov_b32_e32 v26, v21
	v_mov_b32_e32 v29, v28
	v_mov_b32_e32 v27, v23
	v_mov_b32_e32 v31, v30
	v_permlane32_swap_b32_e32 v16, v19
	v_permlane32_swap_b32_e32 v17, v20
	v_permlane32_swap_b32_e32 v18, v22
	v_permlane32_swap_b32_e32 v21, v26
	v_permlane32_swap_b32_e32 v28, v29
	v_permlane32_swap_b32_e32 v23, v27
	s_waitcnt vmcnt(2)
	v_pk_mul_f32 v[6:7], v[6:7], v[56:57]
	v_pk_mul_f32 v[4:5], v[4:5], v[54:55]
	v_pk_fma_f32 v[2:3], v[2:3], v[40:41], v[6:7]
	v_pk_fma_f32 v[0:1], v[0:1], v[38:39], v[4:5]
	v_permlane32_swap_b32_e32 v30, v31
	s_waitcnt vmcnt(1)
	v_pk_fma_f32 v[2:3], v[14:15], v[44:45], v[2:3]
	v_pk_fma_f32 v[0:1], v[12:13], v[42:43], v[0:1]
	s_waitcnt vmcnt(0)
	v_pk_fma_f32 v[2:3], v[10:11], v[34:35], v[2:3]
	v_pk_fma_f32 v[0:1], v[8:9], v[32:33], v[0:1]
	s_nop 0
	v_add_f32_e32 v0, v0, v1
	v_add_f32_e32 v1, v2, v3
	v_add_f32_e32 v0, v0, v1
	s_nop 1
	v_add_f32_dpp v0, v0, v0 quad_perm:[1,0,3,2] row_mask:0xf bank_mask:0xf bound_ctrl:1
	s_nop 1
	v_add_f32_dpp v0, v0, v0 quad_perm:[2,3,0,1] row_mask:0xf bank_mask:0xf bound_ctrl:1
	s_nop 1
	v_add_f32_dpp v0, v0, v0 row_ror:4 row_mask:0xf bank_mask:0xf bound_ctrl:1
	s_nop 1
	v_add_f32_dpp v0, v0, v0 row_ror:8 row_mask:0xf bank_mask:0xf bound_ctrl:1
	v_mov_b32_e32 v1, v0
	s_nop 1
	v_permlane16_swap_b32_e32 v0, v1
	v_add_f32_e32 v0, v0, v1
	v_mov_b32_e32 v1, v0
	s_nop 1
	v_permlane32_swap_b32_e32 v0, v1
	s_and_saveexec_b64 s[0:1], vcc
	s_cbranch_execz .LBB1_4
	v_add_f32_e32 v6, v16, v19
	v_cmp_eq_u32_e32 vcc, 0, v24
	v_add_f32_e32 v5, v17, v20
	v_add_f32_e32 v4, v18, v22
	v_cndmask_b32_e32 v6, 0, v6, vcc
	v_cmp_eq_u32_e32 vcc, 1, v24
	v_add_f32_e32 v3, v21, v26
	v_add_f32_e32 v2, v28, v29
	v_cndmask_b32_e32 v5, v6, v5, vcc
	v_cmp_eq_u32_e32 vcc, 2, v24
	v_add_f32_e32 v0, v0, v1
	v_add_f32_e32 v1, v30, v31
	v_cndmask_b32_e32 v4, v5, v4, vcc
	v_cmp_eq_u32_e32 vcc, 3, v24
	s_lshl_b32 s0, s8, 13
	s_and_b32 s0, s0, 0x1e000
	v_cndmask_b32_e32 v3, v4, v3, vcc
	v_cmp_eq_u32_e32 vcc, 4, v24
	s_add_u32 s0, s6, s0
	s_addc_u32 s1, s7, 0
	v_cndmask_b32_e32 v2, v3, v2, vcc
	v_add_f32_e32 v3, v23, v27
	v_cmp_eq_u32_e32 vcc, 5, v24
	s_nop 1
	v_cndmask_b32_e32 v2, v2, v3, vcc
	v_cmp_eq_u32_e32 vcc, 6, v24
	s_nop 1
	v_cndmask_b32_e32 v1, v2, v1, vcc
	v_cmp_eq_u32_e32 vcc, 7, v24
	s_nop 1
	v_cndmask_b32_e32 v2, v1, v0, vcc
	v_add_u32_e32 v0, s9, v25
	v_ashrrev_i32_e32 v0, 4, v0
	v_ashrrev_i32_e32 v1, 31, v0
	v_lshl_add_u64 v[0:1], v[0:1], 2, s[0:1]
	v_add_co_u32_e32 v0, vcc, 0x6000, v0
	s_nop 1
	v_addc_co_u32_e32 v1, vcc, 0, v1, vcc
	global_store_dword v[0:1], v2, off offset:64

	.amdhsa_kernel _Z13stream_kernelPKfPf
		.amdhsa_group_segment_fixed_size 4096
		.amdhsa_private_segment_fixed_size 0
		.amdhsa_kernarg_size 16
		.amdhsa_user_sgpr_count 2
		.amdhsa_user_sgpr_dispatch_ptr 0
		.amdhsa_user_sgpr_queue_ptr 0
		.amdhsa_user_sgpr_kernarg_segment_ptr 1
		.amdhsa_user_sgpr_dispatch_id 0
		.amdhsa_user_sgpr_kernarg_preload_length 0
		.amdhsa_user_sgpr_kernarg_preload_offset 0
		.amdhsa_user_sgpr_private_segment_size 0
		.amdhsa_uses_dynamic_stack 0
		.amdhsa_enable_private_segment 0
		.amdhsa_system_sgpr_workgroup_id_x 1
		.amdhsa_system_sgpr_workgroup_id_y 0
		.amdhsa_system_sgpr_workgroup_id_z 0
		.amdhsa_system_sgpr_workgroup_info 0
		.amdhsa_system_vgpr_workitem_id 0
		.amdhsa_next_free_vgpr 67
		.amdhsa_next_free_sgpr 12
		.amdhsa_accum_offset 68
		.amdhsa_reserve_vcc 1
		.amdhsa_float_round_mode_32 0
		.amdhsa_float_round_mode_16_64 0
		.amdhsa_float_denorm_mode_32 3
		.amdhsa_float_denorm_mode_16_64 3
		.amdhsa_dx10_clamp 1
		.amdhsa_ieee_mode 1
		.amdhsa_fp16_overflow 0
		.amdhsa_tg_split 0
		.amdhsa_exception_fp_ieee_invalid_op 0
		.amdhsa_exception_fp_denorm_src 0
		.amdhsa_exception_fp_ieee_div_zero 0
		.amdhsa_exception_fp_ieee_overflow 0
		.amdhsa_exception_fp_ieee_underflow 0
		.amdhsa_exception_fp_ieee_inexact 0
		.amdhsa_exception_int_div_zero 0
	.end_amdhsa_kernel

.Lfunc_end1:
	.size	_Z13stream_kernelPKfPf, .Lfunc_end1-_Z13stream_kernelPKfPf
	.set _Z13stream_kernelPKfPf.num_vgpr, 67
	.set _Z13stream_kernelPKfPf.num_agpr, 0
	.set _Z13stream_kernelPKfPf.numbered_sgpr, 12
	.set _Z13stream_kernelPKfPf.num_named_barrier, 0
	.set _Z13stream_kernelPKfPf.private_seg_size, 0
	.set _Z13stream_kernelPKfPf.uses_vcc, 1
	.set _Z13stream_kernelPKfPf.uses_flat_scratch, 0
	.set _Z13stream_kernelPKfPf.has_dyn_sized_stack, 0
	.set _Z13stream_kernelPKfPf.has_recursion, 0
	.set _Z13stream_kernelPKfPf.has_indirect_call, 0

amdhsa.kernels:
  - .agpr_count:     0
    .args:
      - .actual_access:  read_only
        .address_space:  global
        .offset:         0
        .size:           8
        .value_kind:     global_buffer
      - .actual_access:  read_only
        .address_space:  global
        .offset:         8
        .size:           8
        .value_kind:     global_buffer
      - .actual_access:  read_only
        .address_space:  global
        .offset:         16
        .size:           8
        .value_kind:     global_buffer
      - .actual_access:  read_only
        .address_space:  global
        .offset:         24
        .size:           8
        .value_kind:     global_buffer
      - .actual_access:  write_only
        .address_space:  global
        .offset:         32
        .size:           8
        .value_kind:     global_buffer
    .group_segment_fixed_size: 2112
    .kernarg_segment_align: 8
    .kernarg_segment_size: 40
    .language:       OpenCL C
    .language_version:
      - 2
      - 0
    .max_flat_workgroup_size: 1024
    .name:           _Z11prep_kernelPKfS0_S0_S0_Pf
    .private_segment_fixed_size: 0
    .sgpr_count:     32
    .sgpr_spill_count: 0
    .symbol:         _Z11prep_kernelPKfS0_S0_S0_Pf.kd
    .uniform_work_group_size: 1
    .uses_dynamic_stack: false
    .vgpr_count:     40
    .vgpr_spill_count: 0
    .wavefront_size: 64
  - .agpr_count:     0
    .args:
      - .actual_access:  read_only
        .address_space:  global
        .offset:         0
        .size:           8
        .value_kind:     global_buffer
      - .address_space:  global
        .offset:         8
        .size:           8
        .value_kind:     global_buffer
    .group_segment_fixed_size: 4096
    .kernarg_segment_align: 8
    .kernarg_segment_size: 16
    .language:       OpenCL C
    .language_version:
      - 2
      - 0
    .max_flat_workgroup_size: 1024
    .name:           _Z13stream_kernelPKfPf
    .private_segment_fixed_size: 0
    .sgpr_count:     18
    .sgpr_spill_count: 0
    .symbol:         _Z13stream_kernelPKfPf.kd
    .uniform_work_group_size: 1
    .uses_dynamic_stack: false
    .vgpr_count:     67
    .vgpr_spill_count: 0
    .wavefront_size: 64
  - .agpr_count:     0
    .args:
      - .actual_access:  read_only
        .address_space:  global
        .offset:         0
        .size:           8
        .value_kind:     global_buffer
      - .actual_access:  write_only
        .address_space:  global
        .offset:         8
        .size:           8
        .value_kind:     global_buffer
    .group_segment_fixed_size: 32
    .kernarg_segment_align: 8
    .kernarg_segment_size: 16
    .language:       OpenCL C
    .language_version:
      - 2
      - 0
    .max_flat_workgroup_size: 256
    .name:           _Z14softmax_kernelPKfPf
    .private_segment_fixed_size: 0
    .sgpr_count:     16
    .sgpr_spill_count: 0
    .symbol:         _Z14softmax_kernelPKfPf.kd
    .uniform_work_group_size: 1
    .uses_dynamic_stack: false
    .vgpr_count:     17
    .vgpr_spill_count: 0
    .wavefront_size: 64
